# write-through (sc0 sc1) stores for q16 (prep_all) and xT (attn_k) so the next kernel does not inherit dirty L2 lines; on top of KV2 loader/epilogue rewrites and prep block rotation
# speedup vs baseline: 1.0062x; 1.0062x over previous
.LBB0_40:
	s_load_dwordx2 s[6:7], s[0:1], 0x48
	s_load_dwordx2 s[4:5], s[0:1], 0x70
	s_lshl_b32 s0, s2, 6
	s_and_b32 s8, s0, 0xfc0
	s_ashr_i32 s0, s2, 10
	s_ashr_i32 s1, s0, 31
	s_and_b32 s9, s2, 0x3c0
	s_lshl_b64 s[2:3], s[0:1], 24
	s_waitcnt lgkmcnt(0)
	s_add_u32 s2, s6, s2
	s_addc_u32 s3, s7, s3
	s_lshl_b32 s6, s9, 14
	s_add_u32 s2, s2, s6
	s_addc_u32 s3, s3, 0
	s_lshl_b32 s6, s8, 2
	s_add_u32 s2, s2, s6
	v_lshlrev_b32_e32 v1, 4, v0
	s_addc_u32 s3, s3, 0
	v_and_b32_e32 v18, 0xf0, v1
	v_mov_b32_e32 v19, 0
	v_lshrrev_b32_e32 v1, 4, v0
	v_or_b32_e32 v20, 0x100, v0
	v_lshl_add_u64 v[14:15], s[2:3], 0, v[18:19]
	v_lshlrev_b32_e32 v2, 14, v1
	v_mov_b32_e32 v3, v19
	v_lshrrev_b32_e32 v21, 4, v20
	v_lshl_add_u64 v[10:11], v[14:15], 0, v[2:3]
	v_lshlrev_b32_e32 v2, 14, v21
	v_lshl_add_u64 v[12:13], v[14:15], 0, v[2:3]
	global_load_dwordx4 v[2:5], v[10:11], off nt
	global_load_dwordx4 v[6:9], v[12:13], off nt
	v_or_b32_e32 v10, 0x200, v0
	v_lshrrev_b32_e32 v22, 4, v10
	v_lshlrev_b32_e32 v10, 14, v22
	v_mov_b32_e32 v11, v19
	v_or_b32_e32 v16, 0x300, v0
	v_lshl_add_u64 v[10:11], v[14:15], 0, v[10:11]
	v_lshrrev_b32_e32 v23, 4, v16
	global_load_dwordx4 v[10:13], v[10:11], off nt
	v_lshlrev_b32_e32 v16, 14, v23
	v_mov_b32_e32 v17, v19
	v_lshl_add_u64 v[14:15], v[14:15], 0, v[16:17]
	global_load_dwordx4 v[14:17], v[14:15], off nt
	s_lshl_b64 s[0:1], s[0:1], 23
	s_movk_i32 s2, 0x104
	s_add_u32 s0, s4, s0
	v_mad_u32_u24 v1, v1, s2, v18
	v_mad_u32_u24 v27, v21, s2, v18
	v_mad_u32_u24 v28, v22, s2, v18
	v_mad_u32_u24 v29, v23, s2, v18
	s_addc_u32 s1, s5, s1
	s_lshl_b32 s2, s8, 11
	s_add_u32 s0, s0, s2
	v_and_b32_e32 v24, 7, v0
	v_lshrrev_b32_e32 v0, 3, v0
	v_lshrrev_b32_e32 v26, 3, v20
	s_addc_u32 s1, s1, 0
	s_lshl_b32 s2, s9, 1
	s_movk_i32 s3, 0x820
	v_lshlrev_b32_e32 v25, 2, v0
	v_lshlrev_b32_e32 v18, 2, v26
	s_add_u32 s0, s0, s2
	v_mad_u32_u24 v25, v24, s3, v25
	v_mad_u32_u24 v31, v24, s3, v18
	v_lshlrev_b32_e32 v18, 4, v24
	s_addc_u32 s1, s1, 0
	v_add_u32_e32 v30, 0x400, v25
	v_add_u32_e32 v32, 0x400, v31
	v_lshl_add_u64 v[20:21], s[0:1], 0, v[18:19]
	v_lshlrev_b32_e32 v18, 11, v0
	v_lshl_add_u64 v[22:23], v[20:21], 0, v[18:19]
	v_lshlrev_b32_e32 v18, 11, v26
	s_waitcnt vmcnt(3)
	ds_write2_b32 v1, v2, v3 offset1:1
	ds_write2_b32 v1, v4, v5 offset0:2 offset1:3
	s_waitcnt vmcnt(2)
	ds_write2_b32 v27, v6, v7 offset1:1
	ds_write2_b32 v27, v8, v9 offset0:2 offset1:3
	s_waitcnt vmcnt(1)
	ds_write2_b32 v28, v10, v11 offset1:1
	ds_write2_b32 v28, v12, v13 offset0:2 offset1:3
	s_waitcnt vmcnt(0)
	ds_write2_b32 v29, v14, v15 offset1:1
	ds_write2_b32 v29, v16, v17 offset0:2 offset1:3
	s_waitcnt lgkmcnt(0)
	s_barrier
	ds_read2_b32 v[4:5], v25 offset1:65
	ds_read2_b32 v[0:1], v25 offset0:130 offset1:195
	ds_read2_b32 v[6:7], v30 offset0:4 offset1:69
	ds_read2_b32 v[2:3], v30 offset0:134 offset1:199
	ds_read2_b32 v[8:9], v31 offset1:65
	ds_read2_b32 v[10:11], v31 offset0:130 offset1:195
	ds_read2_b32 v[12:13], v32 offset0:4 offset1:69
	ds_read2_b32 v[14:15], v32 offset0:134 offset1:199
	s_waitcnt lgkmcnt(4)
	v_cvt_pk_f16_f32 v3, v2, v3
	v_cvt_pk_f16_f32 v2, v6, v7
	v_cvt_pk_f16_f32 v1, v0, v1
	v_cvt_pk_f16_f32 v0, v4, v5
	s_waitcnt lgkmcnt(0)
	v_cvt_pk_f16_f32 v7, v14, v15
	v_cvt_pk_f16_f32 v6, v12, v13
	v_cvt_pk_f16_f32 v5, v10, v11
	v_cvt_pk_f16_f32 v4, v8, v9
	global_store_dwordx4 v[22:23], v[0:3], off sc0 sc1
	s_nop 1
	v_lshl_add_u64 v[0:1], v[20:21], 0, v[18:19]
	global_store_dwordx4 v[0:1], v[4:7], off sc0 sc1
	s_endpgm

.LBB5_1:
	ds_read_b128 v[0:3], v186
	ds_read_b128 v[4:7], v186 offset:4096
	ds_read_b128 v[8:11], v187
	ds_read_b128 v[12:15], v187 offset:4096
	ds_read_b128 v[16:19], v188
	ds_read_b128 v[20:23], v188 offset:4096
	ds_read_b128 v[24:27], v189
	ds_read_b128 v[28:31], v189 offset:4096
	ds_read_b128 v[64:67], v186 offset:8192
	ds_read_b128 v[68:71], v186 offset:12288
	ds_read_b128 v[72:75], v187 offset:8192
	ds_read_b128 v[76:79], v187 offset:12288
	ds_read_b128 v[80:83], v188 offset:8192
	ds_read_b128 v[84:87], v188 offset:12288
	ds_read_b128 v[88:91], v189 offset:8192
	ds_read_b128 v[160:163], v189 offset:12288
	s_waitcnt lgkmcnt(14)
	v_mfma_f32_32x32x16_f16 v[48:63], v[0:3], v[120:123], 0
	ds_read_b128 v[152:155], v190 offset:32768
	ds_read_b128 v[156:159], v190 offset:49152
	ds_read_b128 v[148:151], v191 offset:32768
	ds_read_b128 v[144:147], v191 offset:49152
	ds_read_b128 v[140:143], v192 offset:32768
	ds_read_b128 v[136:139], v192 offset:49152
	ds_read_b128 v[132:135], v193 offset:32768
	ds_read_b128 v[92:95], v193 offset:49152
	v_mfma_f32_32x32x16_f16 v[32:47], v[4:7], v[120:123], 0
	s_waitcnt lgkmcnt(14)
	v_mfma_f32_32x32x16_f16 v[48:63], v[8:11], v[124:127], v[48:63]
	v_mfma_f32_32x32x16_f16 v[32:47], v[12:15], v[124:127], v[32:47]
	v_mfma_f32_32x32x16_f16 v[48:63], v[16:19], v[116:119], v[48:63]
	v_mfma_f32_32x32x16_f16 v[32:47], v[20:23], v[116:119], v[32:47]
	v_mfma_f32_32x32x16_f16 v[48:63], v[24:27], v[112:115], v[48:63]
	v_mfma_f32_32x32x16_f16 v[32:47], v[28:31], v[112:115], v[32:47]
	v_mfma_f32_32x32x16_f16 v[16:31], v[64:67], v[120:123], 0
	s_waitcnt lgkmcnt(13)
	v_mfma_f32_32x32x16_f16 v[16:31], v[72:75], v[124:127], v[16:31]
	v_mfma_f32_32x32x16_f16 v[0:15], v[68:71], v[120:123], 0
	s_waitcnt lgkmcnt(11)
	v_mfma_f32_32x32x16_f16 v[16:31], v[80:83], v[116:119], v[16:31]
	v_mfma_f32_32x32x16_f16 v[0:15], v[76:79], v[124:127], v[0:15]
	s_waitcnt lgkmcnt(9)
	v_mfma_f32_32x32x16_f16 v[16:31], v[88:91], v[112:115], v[16:31]
	v_mfma_f32_32x32x16_f16 v[0:15], v[84:87], v[116:119], v[0:15]
	ds_read_b128 v[128:131], v194 offset:32768
	ds_read_b128 v[88:91], v194 offset:49152
	ds_read_b128 v[84:87], v195 offset:32768
	ds_read_b128 v[80:83], v195 offset:49152
	ds_read_b128 v[76:79], v196 offset:32768
	ds_read_b128 v[72:75], v196 offset:49152
	ds_read_b128 v[68:71], v197 offset:32768
	ds_read_b128 v[64:67], v197 offset:49152
	s_waitcnt lgkmcnt(14)
	v_mfma_f32_32x32x16_f16 v[0:15], v[160:163], v[112:115], v[0:15]
	v_max_f32_e32 v160, v49, v49
	v_max_f32_e32 v161, v48, v48
	s_nop 9
	v_max_f32_e32 v163, v1, v1
	v_max_f32_e32 v164, v0, v0
	v_max_f32_e32 v160, v161, v160
	v_max_f32_e32 v161, v33, v33
	v_max_f32_e32 v162, v32, v32
	v_max_f32_e32 v163, v164, v163
	v_max_f32_e32 v161, v162, v161
	v_max3_f32 v162, v16, v17, v18
	v_max3_f32 v163, v163, v2, v3
	v_max3_f32 v160, v160, v50, v51
	v_max3_f32 v161, v161, v34, v35
	v_max3_f32 v162, v162, v19, v20
	v_max3_f32 v163, v163, v4, v5
	v_max3_f32 v160, v160, v52, v53
	v_max3_f32 v161, v161, v36, v37
	v_max3_f32 v162, v162, v21, v22
	v_max3_f32 v163, v163, v6, v7
	v_max3_f32 v160, v160, v54, v55
	v_max3_f32 v161, v161, v38, v39
	v_max3_f32 v162, v162, v23, v24
	v_max3_f32 v163, v163, v8, v9
	v_max3_f32 v160, v160, v56, v57
	v_max3_f32 v161, v161, v40, v41
	v_max3_f32 v162, v162, v25, v26
	v_max3_f32 v163, v163, v10, v11
	v_max3_f32 v160, v160, v58, v59
	v_max3_f32 v161, v161, v42, v43
	v_max3_f32 v162, v162, v27, v28
	v_max3_f32 v163, v163, v12, v13
	v_max3_f32 v160, v160, v60, v61
	v_max3_f32 v161, v161, v44, v45
	v_max3_f32 v162, v162, v29, v30
	v_max3_f32 v163, v163, v14, v15
	v_max3_f32 v160, v160, v62, v63
	v_max3_f32 v161, v161, v46, v47
	v_max3_f32 v162, v162, v31, v163
	v_max3_f32 v160, v160, v161, v162
	ds_bpermute_b32 v161, v198, v160
	s_waitcnt lgkmcnt(0)
	v_max3_f32 v180, v160, v161, s0
	v_sub_f32_e32 v48, v48, v180
	v_sub_f32_e32 v32, v32, v180
	v_exp_f32_e32 v48, v48
	v_sub_f32_e32 v49, v49, v180
	v_exp_f32_e32 v162, v32
	v_sub_f32_e32 v32, v33, v180
	v_exp_f32_e32 v49, v49
	v_sub_f32_e32 v50, v50, v180
	v_exp_f32_e32 v163, v32
	v_sub_f32_e32 v32, v34, v180
	v_exp_f32_e32 v50, v50
	v_sub_f32_e32 v51, v51, v180
	v_exp_f32_e32 v164, v32
	v_sub_f32_e32 v32, v35, v180
	v_exp_f32_e32 v51, v51
	v_sub_f32_e32 v52, v52, v180
	v_exp_f32_e32 v165, v32
	v_sub_f32_e32 v33, v36, v180
	v_add_f32_e32 v161, 0, v48
	v_exp_f32_e32 v52, v52
	v_sub_f32_e32 v53, v53, v180
	v_add_f32_e32 v32, 0, v162
	v_exp_f32_e32 v36, v33
	v_sub_f32_e32 v33, v37, v180
	v_add_f32_e32 v161, v161, v49
	v_exp_f32_e32 v53, v53
	v_sub_f32_e32 v54, v54, v180
	v_add_f32_e32 v32, v32, v163
	v_exp_f32_e32 v37, v33
	v_sub_f32_e32 v33, v38, v180
	v_add_f32_e32 v161, v161, v50
	v_exp_f32_e32 v54, v54
	v_sub_f32_e32 v55, v55, v180
	v_add_f32_e32 v32, v32, v164
	v_exp_f32_e32 v38, v33
	v_sub_f32_e32 v33, v39, v180
	v_add_f32_e32 v161, v161, v51
	v_exp_f32_e32 v55, v55
	v_sub_f32_e32 v56, v56, v180
	v_add_f32_e32 v32, v32, v165
	v_exp_f32_e32 v39, v33
	v_sub_f32_e32 v33, v40, v180
	v_add_f32_e32 v161, v161, v52
	v_exp_f32_e32 v56, v56
	v_sub_f32_e32 v57, v57, v180
	v_add_f32_e32 v32, v32, v36
	v_exp_f32_e32 v40, v33
	v_sub_f32_e32 v33, v41, v180
	v_add_f32_e32 v161, v161, v53
	v_exp_f32_e32 v57, v57
	v_sub_f32_e32 v58, v58, v180
	v_add_f32_e32 v32, v32, v37
	v_exp_f32_e32 v166, v33
	v_sub_f32_e32 v33, v42, v180
	v_add_f32_e32 v161, v161, v54
	v_exp_f32_e32 v58, v58
	v_sub_f32_e32 v59, v59, v180
	v_add_f32_e32 v32, v32, v38
	v_exp_f32_e32 v41, v33
	v_sub_f32_e32 v33, v43, v180
	v_add_f32_e32 v161, v161, v55
	v_exp_f32_e32 v59, v59
	v_sub_f32_e32 v60, v60, v180
	v_add_f32_e32 v32, v32, v39
	v_exp_f32_e32 v167, v33
	v_sub_f32_e32 v33, v44, v180
	v_add_f32_e32 v161, v161, v56
	v_exp_f32_e32 v60, v60
	v_sub_f32_e32 v61, v61, v180
	v_add_f32_e32 v32, v32, v40
	v_exp_f32_e32 v42, v33
	v_sub_f32_e32 v33, v45, v180
	v_add_f32_e32 v161, v161, v57
	v_exp_f32_e32 v61, v61
	v_sub_f32_e32 v62, v62, v180
	v_add_f32_e32 v32, v32, v166
	v_exp_f32_e32 v44, v33
	v_sub_f32_e32 v33, v46, v180
	v_add_f32_e32 v161, v161, v58
	v_exp_f32_e32 v62, v62
	v_sub_f32_e32 v63, v63, v180
	v_add_f32_e32 v32, v32, v41
	v_exp_f32_e32 v43, v33
	v_sub_f32_e32 v33, v47, v180
	v_add_f32_e32 v161, v161, v59
	v_exp_f32_e32 v63, v63
	v_add_f32_e32 v32, v32, v167
	v_exp_f32_e32 v45, v33
	v_add_f32_e32 v161, v161, v60
	v_add_f32_e32 v32, v32, v42
	v_add_f32_e32 v161, v161, v61
	v_add_f32_e32 v32, v32, v44
	v_add_f32_e32 v161, v161, v62
	v_add_f32_e32 v32, v32, v43
	v_add_f32_e32 v161, v161, v63
	v_add_f32_e32 v32, v32, v45
	v_sub_f32_e32 v16, v16, v180
	v_sub_f32_e32 v0, v0, v180
	v_add_f32_e32 v32, v161, v32
	v_exp_f32_e32 v16, v16
	v_sub_f32_e32 v17, v17, v180
	v_exp_f32_e32 v161, v0
	v_sub_f32_e32 v0, v1, v180
	v_exp_f32_e32 v17, v17
	v_sub_f32_e32 v18, v18, v180
	v_exp_f32_e32 v168, v0
	v_sub_f32_e32 v0, v2, v180
	v_exp_f32_e32 v18, v18
	v_sub_f32_e32 v19, v19, v180
	v_exp_f32_e32 v169, v0
	v_sub_f32_e32 v0, v3, v180
	v_exp_f32_e32 v19, v19
	v_sub_f32_e32 v20, v20, v180
	v_exp_f32_e32 v170, v0
	v_sub_f32_e32 v1, v4, v180
	v_add_f32_e32 v33, 0, v16
	v_exp_f32_e32 v20, v20
	v_sub_f32_e32 v21, v21, v180
	v_add_f32_e32 v0, 0, v161
	v_exp_f32_e32 v4, v1
	v_sub_f32_e32 v1, v5, v180
	v_add_f32_e32 v33, v33, v17
	v_exp_f32_e32 v21, v21
	v_sub_f32_e32 v22, v22, v180
	v_add_f32_e32 v0, v0, v168
	v_exp_f32_e32 v5, v1
	v_sub_f32_e32 v1, v6, v180
	v_add_f32_e32 v33, v33, v18
	v_exp_f32_e32 v22, v22
	v_sub_f32_e32 v23, v23, v180
	v_add_f32_e32 v0, v0, v169
	v_exp_f32_e32 v6, v1
	v_sub_f32_e32 v1, v7, v180
	v_add_f32_e32 v33, v33, v19
	v_exp_f32_e32 v23, v23
	v_sub_f32_e32 v24, v24, v180
	v_add_f32_e32 v0, v0, v170
	v_exp_f32_e32 v7, v1
	v_sub_f32_e32 v1, v8, v180
	v_add_f32_e32 v33, v33, v20
	v_exp_f32_e32 v24, v24
	v_sub_f32_e32 v25, v25, v180
	v_add_f32_e32 v0, v0, v4
	v_exp_f32_e32 v8, v1
	v_sub_f32_e32 v1, v9, v180
	v_add_f32_e32 v33, v33, v21
	v_exp_f32_e32 v25, v25
	v_sub_f32_e32 v26, v26, v180
	v_add_f32_e32 v0, v0, v5
	v_exp_f32_e32 v9, v1
	v_sub_f32_e32 v1, v10, v180
	v_add_f32_e32 v33, v33, v22
	v_exp_f32_e32 v26, v26
	v_sub_f32_e32 v27, v27, v180
	v_add_f32_e32 v0, v0, v6
	v_exp_f32_e32 v10, v1
	v_sub_f32_e32 v1, v11, v180
	v_add_f32_e32 v33, v33, v23
	v_exp_f32_e32 v27, v27
	v_sub_f32_e32 v28, v28, v180
	v_add_f32_e32 v0, v0, v7
	v_exp_f32_e32 v11, v1
	v_sub_f32_e32 v1, v12, v180
	v_add_f32_e32 v33, v33, v24
	v_exp_f32_e32 v28, v28
	v_sub_f32_e32 v29, v29, v180
	v_add_f32_e32 v0, v0, v8
	v_exp_f32_e32 v12, v1
	v_sub_f32_e32 v1, v13, v180
	v_add_f32_e32 v33, v33, v25
	v_exp_f32_e32 v29, v29
	v_sub_f32_e32 v30, v30, v180
	v_add_f32_e32 v0, v0, v9
	v_exp_f32_e32 v13, v1
	v_sub_f32_e32 v1, v14, v180
	v_add_f32_e32 v33, v33, v26
	v_exp_f32_e32 v30, v30
	v_sub_f32_e32 v31, v31, v180
	v_add_f32_e32 v0, v0, v10
	v_exp_f32_e32 v14, v1
	v_sub_f32_e32 v1, v15, v180
	v_add_f32_e32 v33, v33, v27
	v_exp_f32_e32 v31, v31
	v_add_f32_e32 v0, v0, v11
	v_exp_f32_e32 v15, v1
	v_add_f32_e32 v33, v33, v28
	v_add_f32_e32 v0, v0, v12
	v_sub_f32_e32 v160, 0xf149f2ca, v180
	v_add_f32_e32 v33, v33, v29
	v_add_f32_e32 v0, v0, v13
	v_exp_f32_e32 v160, v160
	v_add_f32_e32 v33, v33, v30
	v_add_f32_e32 v0, v0, v14
	v_add_f32_e32 v33, v33, v31
	v_add_f32_e32 v0, v0, v15
	v_add_f32_e32 v0, v33, v0
	v_add_f32_e32 v212, v32, v0
	v_fmac_f32_e32 v212, 0, v160
	v_cvt_pk_f16_f32 v3, v54, v55
	v_cvt_pk_f16_f32 v2, v52, v53
	v_cvt_pk_f16_f32 v1, v50, v51
	v_cvt_pk_f16_f32 v0, v48, v49
	v_cvt_pk_f16_f32 v35, v62, v63
	v_cvt_pk_f16_f32 v34, v60, v61
	v_cvt_pk_f16_f32 v33, v58, v59
	v_cvt_pk_f16_f32 v32, v56, v57
	v_cvt_pk_f16_f32 v39, v38, v39
	v_cvt_pk_f16_f32 v38, v36, v37
	v_cvt_pk_f16_f32 v37, v164, v165
	v_cvt_pk_f16_f32 v36, v162, v163
	v_cvt_pk_f16_f32 v43, v43, v45
	v_cvt_pk_f16_f32 v42, v42, v44
	v_cvt_pk_f16_f32 v41, v41, v167
	v_cvt_pk_f16_f32 v40, v40, v166
	v_cvt_pk_f16_f32 v47, v22, v23
	v_cvt_pk_f16_f32 v46, v20, v21
	v_cvt_pk_f16_f32 v45, v18, v19
	v_cvt_pk_f16_f32 v44, v16, v17
	v_cvt_pk_f16_f32 v51, v30, v31
	v_cvt_pk_f16_f32 v50, v28, v29
	v_cvt_pk_f16_f32 v49, v26, v27
	v_cvt_pk_f16_f32 v48, v24, v25
	v_cvt_pk_f16_f32 v55, v6, v7
	v_cvt_pk_f16_f32 v54, v4, v5
	v_cvt_pk_f16_f32 v53, v169, v170
	v_cvt_pk_f16_f32 v52, v161, v168
	v_cvt_pk_f16_f32 v59, v14, v15
	v_cvt_pk_f16_f32 v58, v12, v13
	v_cvt_pk_f16_f32 v57, v10, v11
	v_cvt_pk_f16_f32 v56, v8, v9
	v_mfma_f32_32x32x16_f16 v[16:31], v[152:155], v[0:3], 0
	v_mfma_f32_32x32x16_f16 v[0:15], v[156:159], v[0:3], 0
	v_mfma_f32_32x32x16_f16 v[16:31], v[148:151], v[32:35], v[16:31]
	v_mfma_f32_32x32x16_f16 v[0:15], v[144:147], v[32:35], v[0:15]
	v_mfma_f32_32x32x16_f16 v[16:31], v[140:143], v[36:39], v[16:31]
	v_mfma_f32_32x32x16_f16 v[0:15], v[136:139], v[36:39], v[0:15]
	v_mfma_f32_32x32x16_f16 v[16:31], v[132:135], v[40:43], v[16:31]
	v_mfma_f32_32x32x16_f16 v[0:15], v[92:95], v[40:43], v[0:15]
	v_mfma_f32_32x32x16_f16 v[16:31], v[128:131], v[44:47], v[16:31]
	v_mfma_f32_32x32x16_f16 v[0:15], v[88:91], v[44:47], v[0:15]
	v_mfma_f32_32x32x16_f16 v[16:31], v[84:87], v[48:51], v[16:31]
	v_mfma_f32_32x32x16_f16 v[0:15], v[80:83], v[48:51], v[0:15]
	v_mfma_f32_32x32x16_f16 v[16:31], v[76:79], v[52:55], v[16:31]
	v_mfma_f32_32x32x16_f16 v[0:15], v[72:75], v[52:55], v[0:15]
	ds_read_b128 v[32:35], v186 offset:16384
	ds_read_b128 v[36:39], v186 offset:20480
	ds_read_b128 v[40:43], v187 offset:16384
	ds_read_b128 v[44:47], v187 offset:20480
	ds_read_b128 v[48:51], v188 offset:16384
	ds_read_b128 v[52:55], v188 offset:20480
	ds_read_b128 v[60:63], v189 offset:16384
	ds_read_b128 v[128:131], v189 offset:20480
	ds_read_b128 v[132:135], v186 offset:24576
	ds_read_b128 v[136:139], v186 offset:28672
	ds_read_b128 v[140:143], v187 offset:24576
	ds_read_b128 v[144:147], v187 offset:28672
	ds_read_b128 v[148:151], v188 offset:24576
	ds_read_b128 v[204:207], v188 offset:28672
	ds_read_b128 v[152:155], v189 offset:24576
	ds_read_b128 v[208:211], v189 offset:28672
	v_mfma_f32_32x32x16_f16 v[16:31], v[68:71], v[56:59], v[16:31]
	v_mfma_f32_32x32x16_f16 v[0:15], v[64:67], v[56:59], v[0:15]
	s_waitcnt lgkmcnt(14)
	v_mfma_f32_32x32x16_f16 v[80:95], v[32:35], v[120:123], 0
	s_waitcnt lgkmcnt(13)
	v_mfma_f32_32x32x16_f16 v[80:95], v[40:43], v[124:127], v[80:95]
	v_mfma_f32_32x32x16_f16 v[64:79], v[36:39], v[120:123], 0
	s_waitcnt lgkmcnt(11)
	v_mfma_f32_32x32x16_f16 v[80:95], v[48:51], v[116:119], v[80:95]
	v_mfma_f32_32x32x16_f16 v[64:79], v[44:47], v[124:127], v[64:79]
	s_waitcnt lgkmcnt(9)
	v_mfma_f32_32x32x16_f16 v[80:95], v[60:63], v[112:115], v[80:95]
	v_mfma_f32_32x32x16_f16 v[64:79], v[52:55], v[116:119], v[64:79]
	s_waitcnt lgkmcnt(7)
	v_mfma_f32_32x32x16_f16 v[48:63], v[132:135], v[120:123], 0
	s_waitcnt lgkmcnt(5)
	v_mfma_f32_32x32x16_f16 v[48:63], v[140:143], v[124:127], v[48:63]
	v_mfma_f32_32x32x16_f16 v[32:47], v[136:139], v[120:123], 0
	s_waitcnt lgkmcnt(3)
	v_mfma_f32_32x32x16_f16 v[48:63], v[148:151], v[116:119], v[48:63]
	v_mfma_f32_32x32x16_f16 v[32:47], v[144:147], v[124:127], v[32:47]
	v_mfma_f32_32x32x16_f16 v[64:79], v[128:131], v[112:115], v[64:79]
	s_waitcnt lgkmcnt(1)
	v_mfma_f32_32x32x16_f16 v[48:63], v[152:155], v[112:115], v[48:63]
	ds_read_b128 v[176:179], v190 offset:33024
	ds_read_b128 v[172:175], v190 offset:49408
	ds_read_b128 v[168:171], v191 offset:33024
	ds_read_b128 v[164:167], v191 offset:49408
	ds_read_b128 v[160:163], v192 offset:33024
	ds_read_b128 v[156:159], v192 offset:49408
	ds_read_b128 v[152:155], v193 offset:33024
	ds_read_b128 v[132:135], v193 offset:49408
	v_mfma_f32_32x32x16_f16 v[32:47], v[204:207], v[116:119], v[32:47]
	ds_read_b128 v[148:151], v194 offset:33024
	ds_read_b128 v[128:131], v194 offset:49408
	ds_read_b128 v[144:147], v195 offset:33024
	ds_read_b128 v[124:127], v195 offset:49408
	ds_read_b128 v[140:143], v196 offset:33024
	ds_read_b128 v[120:123], v196 offset:49408
	ds_read_b128 v[136:139], v197 offset:33024
	ds_read_b128 v[116:119], v197 offset:49408
	s_waitcnt lgkmcnt(14)
	v_mfma_f32_32x32x16_f16 v[32:47], v[208:211], v[112:115], v[32:47]
	v_max_f32_e32 v112, v81, v81
	v_max_f32_e32 v113, v80, v80
	s_nop 9
	v_max_f32_e32 v115, v33, v33
	v_max_f32_e32 v204, v32, v32
	v_max_f32_e32 v112, v113, v112
	v_max_f32_e32 v113, v65, v65
	v_max_f32_e32 v114, v64, v64
	v_max_f32_e32 v115, v204, v115
	v_max_f32_e32 v113, v114, v113
	v_max3_f32 v114, v48, v49, v50
	v_max3_f32 v115, v115, v34, v35
	v_max3_f32 v112, v112, v82, v83
	v_max3_f32 v113, v113, v66, v67
	v_max3_f32 v114, v114, v51, v52
	v_max3_f32 v115, v115, v36, v37
	v_max3_f32 v112, v112, v84, v85
	v_max3_f32 v113, v113, v68, v69
	v_max3_f32 v114, v114, v53, v54
	v_max3_f32 v115, v115, v38, v39
	v_max3_f32 v112, v112, v86, v87
	v_max3_f32 v113, v113, v70, v71
	v_max3_f32 v114, v114, v55, v56
	v_max3_f32 v115, v115, v40, v41
	v_max3_f32 v112, v112, v88, v89
	v_max3_f32 v113, v113, v72, v73
	v_max3_f32 v114, v114, v57, v58
	v_max3_f32 v115, v115, v42, v43
	v_max3_f32 v112, v112, v90, v91
	v_max3_f32 v113, v113, v74, v75
	v_max3_f32 v114, v114, v59, v60
	v_max3_f32 v115, v115, v44, v45
	v_max3_f32 v112, v112, v92, v93
	v_max3_f32 v113, v113, v76, v77
	v_max3_f32 v114, v114, v61, v62
	v_max3_f32 v115, v115, v46, v47
	v_max3_f32 v112, v112, v94, v95
	v_max3_f32 v113, v113, v78, v79
	v_max3_f32 v114, v114, v63, v115
	v_max3_f32 v112, v112, v113, v114
	ds_bpermute_b32 v113, v198, v112
	s_waitcnt lgkmcnt(0)
	v_max3_f32 v113, v180, v112, v113
	v_sub_f32_e32 v49, v49, v113
	v_exp_f32_e32 v205, v49
	v_sub_f32_e32 v49, v50, v113
	v_sub_f32_e32 v50, v51, v113
	v_sub_f32_e32 v51, v52, v113
	v_exp_f32_e32 v52, v51
	v_sub_f32_e32 v51, v53, v113
	v_exp_f32_e32 v53, v51
	v_sub_f32_e32 v51, v54, v113
	v_sub_f32_e32 v54, v55, v113
	v_sub_f32_e32 v55, v56, v113
	v_exp_f32_e32 v56, v55
	v_sub_f32_e32 v55, v57, v113
	v_exp_f32_e32 v57, v55
	v_sub_f32_e32 v55, v58, v113
	v_exp_f32_e32 v58, v55
	v_sub_f32_e32 v55, v59, v113
	v_exp_f32_e32 v59, v55
	v_sub_f32_e32 v55, v60, v113
	v_sub_f32_e32 v80, v80, v113
	v_sub_f32_e32 v64, v64, v113
	v_sub_f32_e32 v48, v48, v113
	v_exp_f32_e32 v60, v55
	v_sub_f32_e32 v55, v61, v113
	v_sub_f32_e32 v32, v32, v113
	v_sub_f32_e32 v112, v180, v113
	v_exp_f32_e32 v114, v80
	v_sub_f32_e32 v80, v81, v113
	v_exp_f32_e32 v180, v64
	v_sub_f32_e32 v64, v65, v113
	v_exp_f32_e32 v48, v48
	v_exp_f32_e32 v61, v55
	v_sub_f32_e32 v55, v62, v113
	v_sub_f32_e32 v62, v63, v113
	v_exp_f32_e32 v63, v32
	v_sub_f32_e32 v32, v33, v113
	v_exp_f32_e32 v115, v80
	v_sub_f32_e32 v80, v82, v113
	v_exp_f32_e32 v204, v64
	v_sub_f32_e32 v64, v66, v113
	v_exp_f32_e32 v207, v32
	v_sub_f32_e32 v32, v34, v113
	v_exp_f32_e32 v82, v80
	v_sub_f32_e32 v80, v83, v113
	v_exp_f32_e32 v66, v64
	v_sub_f32_e32 v64, v67, v113
	v_exp_f32_e32 v49, v49
	v_exp_f32_e32 v208, v32
	v_sub_f32_e32 v32, v35, v113
	v_exp_f32_e32 v83, v80
	v_sub_f32_e32 v81, v84, v113
	v_exp_f32_e32 v67, v64
	v_sub_f32_e32 v65, v68, v113
	v_exp_f32_e32 v206, v50
	v_exp_f32_e32 v209, v32
	v_sub_f32_e32 v33, v36, v113
	v_add_f32_e32 v80, 0, v114
	v_exp_f32_e32 v84, v81
	v_sub_f32_e32 v81, v85, v113
	v_add_f32_e32 v64, 0, v180
	v_exp_f32_e32 v68, v65
	v_sub_f32_e32 v65, v69, v113
	v_add_f32_e32 v50, 0, v48
	v_add_f32_e32 v32, 0, v63
	v_exp_f32_e32 v210, v33
	v_sub_f32_e32 v33, v37, v113
	v_add_f32_e32 v80, v80, v115
	v_exp_f32_e32 v85, v81
	v_sub_f32_e32 v81, v86, v113
	v_add_f32_e32 v64, v64, v204
	v_exp_f32_e32 v69, v65
	v_sub_f32_e32 v65, v70, v113
	v_add_f32_e32 v50, v50, v205
	v_add_f32_e32 v32, v32, v207
	v_exp_f32_e32 v211, v33
	v_sub_f32_e32 v33, v38, v113
	v_add_f32_e32 v80, v80, v82
	v_exp_f32_e32 v86, v81
	v_sub_f32_e32 v81, v87, v113
	v_add_f32_e32 v64, v64, v66
	v_exp_f32_e32 v70, v65
	v_sub_f32_e32 v65, v71, v113
	v_add_f32_e32 v50, v50, v49
	v_exp_f32_e32 v51, v51
	v_add_f32_e32 v32, v32, v208
	v_exp_f32_e32 v213, v33
	v_sub_f32_e32 v33, v39, v113
	v_add_f32_e32 v80, v80, v83
	v_exp_f32_e32 v87, v81
	v_sub_f32_e32 v81, v88, v113
	v_add_f32_e32 v64, v64, v67
	v_exp_f32_e32 v71, v65
	v_sub_f32_e32 v65, v72, v113
	v_add_f32_e32 v50, v50, v206
	v_exp_f32_e32 v54, v54
	v_add_f32_e32 v32, v32, v209
	v_exp_f32_e32 v214, v33
	v_sub_f32_e32 v33, v40, v113
	v_add_f32_e32 v80, v80, v84
	v_exp_f32_e32 v88, v81
	v_sub_f32_e32 v81, v89, v113
	v_add_f32_e32 v64, v64, v68
	v_exp_f32_e32 v72, v65
	v_sub_f32_e32 v65, v73, v113
	v_add_f32_e32 v50, v50, v52
	v_add_f32_e32 v32, v32, v210
	v_exp_f32_e32 v215, v33
	v_sub_f32_e32 v33, v41, v113
	v_add_f32_e32 v80, v80, v85
	v_exp_f32_e32 v89, v81
	v_sub_f32_e32 v81, v90, v113
	v_add_f32_e32 v64, v64, v69
	v_exp_f32_e32 v73, v65
	v_sub_f32_e32 v65, v74, v113
	v_add_f32_e32 v50, v50, v53
	v_add_f32_e32 v32, v32, v211
	v_exp_f32_e32 v216, v33
	v_sub_f32_e32 v33, v42, v113
	v_add_f32_e32 v80, v80, v86
	v_exp_f32_e32 v90, v81
	v_sub_f32_e32 v81, v91, v113
	v_add_f32_e32 v64, v64, v70
	v_exp_f32_e32 v74, v65
	v_sub_f32_e32 v65, v75, v113
	v_add_f32_e32 v50, v50, v51
	v_add_f32_e32 v32, v32, v213
	v_exp_f32_e32 v217, v33
	v_sub_f32_e32 v33, v43, v113
	v_add_f32_e32 v80, v80, v87
	v_exp_f32_e32 v91, v81
	v_sub_f32_e32 v81, v92, v113
	v_add_f32_e32 v64, v64, v71
	v_exp_f32_e32 v75, v65
	v_sub_f32_e32 v65, v76, v113
	v_add_f32_e32 v50, v50, v54
	v_add_f32_e32 v32, v32, v214
	v_exp_f32_e32 v218, v33
	v_sub_f32_e32 v33, v44, v113
	v_add_f32_e32 v80, v80, v88
	v_exp_f32_e32 v92, v81
	v_sub_f32_e32 v81, v93, v113
	v_add_f32_e32 v64, v64, v72
	v_exp_f32_e32 v76, v65
	v_sub_f32_e32 v65, v77, v113
	v_add_f32_e32 v50, v50, v56
	v_add_f32_e32 v32, v32, v215
	v_exp_f32_e32 v219, v33
	v_sub_f32_e32 v33, v45, v113
	v_add_f32_e32 v80, v80, v89
	v_exp_f32_e32 v93, v81
	v_sub_f32_e32 v81, v94, v113
	v_add_f32_e32 v64, v64, v73
	v_exp_f32_e32 v77, v65
	v_sub_f32_e32 v65, v78, v113
	v_add_f32_e32 v50, v50, v57
	v_add_f32_e32 v32, v32, v216
	v_exp_f32_e32 v220, v33
	v_sub_f32_e32 v33, v46, v113
	v_add_f32_e32 v80, v80, v90
	v_exp_f32_e32 v94, v81
	v_sub_f32_e32 v81, v95, v113
	v_add_f32_e32 v64, v64, v74
	v_exp_f32_e32 v78, v65
	v_sub_f32_e32 v65, v79, v113
	v_add_f32_e32 v50, v50, v58
	v_exp_f32_e32 v55, v55
	v_add_f32_e32 v32, v32, v217
	v_exp_f32_e32 v221, v33
	v_sub_f32_e32 v33, v47, v113
	v_add_f32_e32 v80, v80, v91
	v_exp_f32_e32 v95, v81
	v_add_f32_e32 v64, v64, v75
	v_exp_f32_e32 v79, v65
	v_add_f32_e32 v50, v50, v59
	v_exp_f32_e32 v62, v62
	v_add_f32_e32 v32, v32, v218
	v_exp_f32_e32 v113, v33
	v_add_f32_e32 v80, v80, v92
	v_add_f32_e32 v64, v64, v76
	v_add_f32_e32 v50, v50, v60
	v_add_f32_e32 v32, v32, v219
	v_add_f32_e32 v80, v80, v93
	v_add_f32_e32 v64, v64, v77
	v_add_f32_e32 v50, v50, v61
	v_add_f32_e32 v32, v32, v220
	v_exp_f32_e32 v112, v112
	v_add_f32_e32 v80, v80, v94
	v_add_f32_e32 v64, v64, v78
	v_add_f32_e32 v50, v50, v55
	v_add_f32_e32 v32, v32, v221
	v_add_f32_e32 v80, v80, v95
	v_add_f32_e32 v64, v64, v79
	v_add_f32_e32 v81, v50, v62
	v_add_f32_e32 v65, v32, v113
	v_pk_add_f32 v[32:33], v[80:81], v[64:65]
	v_cvt_pk_f16_f32 v35, v86, v87
	v_add_f32_e32 v64, v32, v33
	v_fmac_f32_e32 v64, v212, v112
	v_cvt_pk_f16_f32 v34, v84, v85
	v_cvt_pk_f16_f32 v33, v82, v83
	v_cvt_pk_f16_f32 v32, v114, v115
	v_cvt_pk_f16_f32 v39, v94, v95
	v_cvt_pk_f16_f32 v38, v92, v93
	v_cvt_pk_f16_f32 v37, v90, v91
	v_cvt_pk_f16_f32 v36, v88, v89
	v_cvt_pk_f16_f32 v43, v70, v71
	v_cvt_pk_f16_f32 v42, v68, v69
	v_cvt_pk_f16_f32 v41, v66, v67
	v_cvt_pk_f16_f32 v40, v180, v204
	v_cvt_pk_f16_f32 v47, v78, v79
	v_cvt_pk_f16_f32 v46, v76, v77
	v_cvt_pk_f16_f32 v45, v74, v75
	v_cvt_pk_f16_f32 v44, v72, v73
	v_cvt_pk_f16_f32 v51, v51, v54
	v_cvt_pk_f16_f32 v50, v52, v53
	v_cvt_pk_f16_f32 v49, v49, v206
	v_cvt_pk_f16_f32 v48, v48, v205
	v_cvt_pk_f16_f32 v55, v55, v62
	v_cvt_pk_f16_f32 v54, v60, v61
	v_cvt_pk_f16_f32 v53, v58, v59
	v_cvt_pk_f16_f32 v52, v56, v57
	v_cvt_pk_f16_f32 v59, v213, v214
	v_cvt_pk_f16_f32 v58, v210, v211
	v_cvt_pk_f16_f32 v57, v208, v209
	v_cvt_pk_f16_f32 v56, v63, v207
	v_cvt_pk_f16_f32 v63, v221, v113
	v_cvt_pk_f16_f32 v62, v219, v220
	v_cvt_pk_f16_f32 v61, v217, v218
	v_cvt_pk_f16_f32 v60, v215, v216
	v_pk_mul_f32 v[30:31], v[112:113], v[30:31] op_sel_hi:[0,1]
	v_pk_mul_f32 v[28:29], v[112:113], v[28:29] op_sel_hi:[0,1]
	v_pk_mul_f32 v[26:27], v[112:113], v[26:27] op_sel_hi:[0,1]
	v_pk_mul_f32 v[24:25], v[112:113], v[24:25] op_sel_hi:[0,1]
	v_pk_mul_f32 v[22:23], v[112:113], v[22:23] op_sel_hi:[0,1]
	v_pk_mul_f32 v[20:21], v[112:113], v[20:21] op_sel_hi:[0,1]
	v_pk_mul_f32 v[18:19], v[112:113], v[18:19] op_sel_hi:[0,1]
	v_pk_mul_f32 v[16:17], v[112:113], v[16:17] op_sel_hi:[0,1]
	v_pk_mul_f32 v[14:15], v[112:113], v[14:15] op_sel_hi:[0,1]
	v_pk_mul_f32 v[12:13], v[112:113], v[12:13] op_sel_hi:[0,1]
	v_mfma_f32_32x32x16_f16 v[16:31], v[176:179], v[32:35], v[16:31]
	v_mul_f32_e64 v10, v112, v10
	v_mul_f32_e64 v11, v112, v11
	v_mul_f32_e64 v8, v112, v8
	v_mul_f32_e64 v9, v112, v9
	v_mul_f32_e64 v6, v112, v6
	v_mul_f32_e64 v7, v112, v7
	v_pk_mul_f32 v[4:5], v[112:113], v[4:5] op_sel_hi:[0,1]
	v_pk_mul_f32 v[2:3], v[112:113], v[2:3] op_sel_hi:[0,1]
	v_pk_mul_f32 v[0:1], v[112:113], v[0:1] op_sel_hi:[0,1]
	v_add_u32_e32 v180, s1, v200
	v_mfma_f32_32x32x16_f16 v[16:31], v[168:171], v[36:39], v[16:31]
	s_addk_i32 s1, 0x100
	s_waitcnt vmcnt(0)
	v_mov_b64_e32 v[114:115], v[110:111]
	s_cmpk_eq_i32 s1, 0x400
	v_mov_b64_e32 v[112:113], v[108:109]
	v_mfma_f32_32x32x16_f16 v[16:31], v[160:163], v[40:43], v[16:31]
	v_mfma_f32_32x32x16_f16 v[0:15], v[172:175], v[32:35], v[0:15]
	ds_bpermute_b32 v32, v198, v64
	s_waitcnt lgkmcnt(0)
	v_add_f32_e32 v32, v64, v32
	v_div_scale_f32 v33, s[2:3], v32, v32, 1.0
	v_mfma_f32_32x32x16_f16 v[16:31], v[152:155], v[44:47], v[16:31]
	v_rcp_f32_e32 v34, v33
	s_nop 0
	v_fma_f32 v35, -v33, v34, 1.0
	v_fmac_f32_e32 v34, v35, v34
	v_div_scale_f32 v35, vcc, 1.0, v32, 1.0
	v_mfma_f32_32x32x16_f16 v[0:15], v[164:167], v[36:39], v[0:15]
	v_mul_f32_e32 v36, v35, v34
	v_fma_f32 v37, -v33, v36, v35
	v_fmac_f32_e32 v36, v37, v34
	v_fma_f32 v33, -v33, v36, v35
	v_div_fmas_f32 v33, v33, v34, v36
	v_div_fixup_f32 v32, v33, v32, 1.0
	v_mfma_f32_32x32x16_f16 v[16:31], v[148:151], v[48:51], v[16:31]
	v_mfma_f32_32x32x16_f16 v[0:15], v[156:159], v[40:43], v[0:15]
	v_mfma_f32_32x32x16_f16 v[16:31], v[144:147], v[52:55], v[16:31]
	v_mfma_f32_32x32x16_f16 v[0:15], v[132:135], v[44:47], v[0:15]
	v_mfma_f32_32x32x16_f16 v[16:31], v[140:143], v[56:59], v[16:31]
	v_mfma_f32_32x32x16_f16 v[0:15], v[128:131], v[48:51], v[0:15]
	v_mfma_f32_32x32x16_f16 v[16:31], v[136:139], v[60:63], v[16:31]
	v_mfma_f32_32x32x16_f16 v[0:15], v[124:127], v[52:55], v[0:15]
	s_nop 10
	v_fma_mixlo_f16 v33, v32, v16, 0
	v_mov_b32_e32 v16, v17
	v_mov_b32_e32 v17, v18
	v_mul_f32_e64 v16, v32, v16
	v_mul_f32_e64 v17, v32, v17
	v_cvt_pk_f16_f32 v17, v16, v17
	v_fma_mixlo_f16 v18, v32, v19, 0
	v_pack_b32_f16 v16, v33, v17
	v_mfma_f32_32x32x16_f16 v[0:15], v[120:123], v[56:59], v[0:15]
	v_alignbit_b32 v17, v18, v17, 16
	v_mov_b32_e32 v18, v21
	v_mov_b32_e32 v19, v22
	v_mul_f32_e64 v18, v32, v18
	v_mul_f32_e64 v19, v32, v19
	v_fma_mixlo_f16 v20, v32, v20, 0
	v_cvt_pk_f16_f32 v19, v18, v19
	v_pack_b32_f16 v18, v20, v19
	v_fma_mixlo_f16 v20, v32, v23, 0
	v_alignbit_b32 v19, v20, v19, 16
	ds_write2_b64 v201, v[16:17], v[18:19] offset1:2
	v_mov_b32_e32 v16, v25
	v_mov_b32_e32 v17, v26
	v_pk_mul_f32 v[16:17], v[32:33], v[16:17] op_sel_hi:[0,1]
	v_mfma_f32_32x32x16_f16 v[0:15], v[116:119], v[60:63], v[0:15]
	v_fma_mixlo_f16 v18, v32, v24, 0
	v_cvt_pk_f16_f32 v17, v16, v17
	v_pack_b32_f16 v16, v18, v17
	v_fma_mixlo_f16 v18, v32, v27, 0
	v_alignbit_b32 v17, v18, v17, 16
	v_mov_b32_e32 v18, v29
	v_mov_b32_e32 v19, v30
	v_pk_mul_f32 v[18:19], v[32:33], v[18:19] op_sel_hi:[0,1]
	v_fma_mixlo_f16 v20, v32, v28, 0
	v_cvt_pk_f16_f32 v19, v18, v19
	v_pack_b32_f16 v18, v20, v19
	v_fma_mixlo_f16 v20, v32, v31, 0
	v_alignbit_b32 v19, v20, v19, 16
	ds_write2_b64 v201, v[16:17], v[18:19] offset0:4 offset1:6
	v_fma_mixlo_f16 v16, v32, v0, 0
	v_mov_b32_e32 v0, v1
	v_mov_b32_e32 v1, v2
	v_pk_mul_f32 v[0:1], v[32:33], v[0:1] op_sel_hi:[0,1]
	v_cvt_pk_f16_f32 v1, v0, v1
	v_fma_mixlo_f16 v2, v32, v3, 0
	v_pack_b32_f16 v0, v16, v1
	v_alignbit_b32 v1, v2, v1, 16
	v_mov_b32_e32 v2, v5
	v_mov_b32_e32 v3, v6
	v_pk_mul_f32 v[2:3], v[32:33], v[2:3] op_sel_hi:[0,1]
	v_fma_mixlo_f16 v4, v32, v4, 0
	v_cvt_pk_f16_f32 v3, v2, v3
	v_pack_b32_f16 v2, v4, v3
	v_fma_mixlo_f16 v4, v32, v7, 0
	v_alignbit_b32 v3, v4, v3, 16
	ds_write2_b64 v201, v[0:1], v[2:3] offset0:8 offset1:10
	v_mov_b32_e32 v0, v9
	v_mov_b32_e32 v1, v10
	v_pk_mul_f32 v[0:1], v[32:33], v[0:1] op_sel_hi:[0,1]
	v_fma_mixlo_f16 v2, v32, v8, 0
	v_cvt_pk_f16_f32 v1, v0, v1
	v_pack_b32_f16 v0, v2, v1
	v_fma_mixlo_f16 v2, v32, v11, 0
	v_alignbit_b32 v1, v2, v1, 16
	v_mov_b32_e32 v2, v13
	v_mov_b32_e32 v3, v14
	v_pk_mul_f32 v[2:3], v[32:33], v[2:3] op_sel_hi:[0,1]
	v_fma_mixlo_f16 v4, v32, v12, 0
	v_cvt_pk_f16_f32 v3, v2, v3
	v_pack_b32_f16 v2, v4, v3
	v_fma_mixlo_f16 v4, v32, v15, 0
	v_alignbit_b32 v3, v4, v3, 16
	ds_write2_b64 v201, v[0:1], v[2:3] offset0:12 offset1:14
	s_waitcnt lgkmcnt(0)
	ds_read_b128 v[0:3], v202
	v_lshlrev_b64 v[4:5], 11, v[180:181]
	v_lshl_add_u64 v[8:9], v[184:185], 0, v[4:5]
	ds_read_b128 v[4:7], v203
	v_mov_b64_e32 v[122:123], v[98:99]
	s_waitcnt lgkmcnt(1)
	global_store_dwordx4 v[8:9], v[0:3], off sc0 sc1
	v_mov_b64_e32 v[126:127], v[102:103]
	v_mov_b64_e32 v[118:119], v[106:107]
	v_add_u32_e32 v0, 8, v180
	v_mov_b32_e32 v1, v181
	v_lshlrev_b64 v[0:1], 11, v[0:1]
	v_lshl_add_u64 v[0:1], v[184:185], 0, v[0:1]
	s_waitcnt lgkmcnt(0)
	global_store_dwordx4 v[0:1], v[4:7], off sc0 sc1
	ds_read_b128 v[0:3], v203 offset:1152
	v_mov_b64_e32 v[120:121], v[96:97]
	v_add_u32_e32 v4, 16, v180
	v_mov_b32_e32 v5, v181
	v_lshlrev_b64 v[4:5], 11, v[4:5]
	v_lshl_add_u64 v[8:9], v[184:185], 0, v[4:5]
	ds_read_b128 v[4:7], v203 offset:2304
	v_add_u32_e32 v180, 24, v180
	s_waitcnt lgkmcnt(1)
	global_store_dwordx4 v[8:9], v[0:3], off sc0 sc1
	v_mov_b64_e32 v[124:125], v[100:101]
	v_mov_b64_e32 v[116:117], v[104:105]
	v_lshlrev_b64 v[0:1], 11, v[180:181]
	v_lshl_add_u64 v[0:1], v[184:185], 0, v[0:1]
	s_waitcnt lgkmcnt(0)
	global_store_dwordx4 v[0:1], v[4:7], off sc0 sc1
	s_waitcnt lgkmcnt(0)
	s_cbranch_scc1 .LBB5_4
